# dense GEMM phases run on the minimal CU count for the same number of rounds (198/176/227); the freed CUs convert expert weights during the whole phase (11/6/19 items each); 4874 items hidden
# speedup vs baseline: 1.0022x; 1.0022x over previous
.LBB0_55:
	s_cmp_lg_u32 s99, 0
	s_cbranch_scc1 .Ltc_itemdone
	v_readlane_b32 s2, v254, 0
	v_readlane_b32 s3, v254, 1
	s_load_dword s0, s[2:3], 0xe8
	s_add_i32 s14, s14, s15
	s_add_i32 s16, s16, s17
	s_add_i32 s10, s10, s18
	s_waitcnt lgkmcnt(0)
	s_add_i32 s22, s22, s0
	s_cmp_lt_i32 s22, 0x14f6
	s_cbranch_scc1 .Ltc_noskip
	s_cmp_ge_i32 s22, 0x2000
	s_cbranch_scc1 .Ltc_noskip
	s_and_b32 s22, s22, 0xff
	s_addk_i32 s22, 0x2000
	s_lshl_b32 s14, s22, 5
	s_lshl_b32 s16, s22, 4
	s_lshl_b32 s10, s22, 9
.Ltc_noskip:
	s_cmpk_lt_i32 s22, 0x2800
	s_cbranch_scc0 .LBB0_60

.Ltc_next:
	s_cmp_ge_u32 s100, 0x130a
	s_cbranch_scc1 .Ltc_alldone
	s_movk_i32 s22, 0x1cf6
	s_cmp_lt_u32 s100, 0xf0a
	s_cselect_b32 s22, 0x10f6, s22
	s_cmp_lt_u32 s100, 0x70a
	s_cselect_b32 s22, 0x24f6, s22
	s_cmp_lt_u32 s100, 0x30a
	s_cselect_b32 s22, 0x14f6, s22
	s_add_i32 s22, s22, s100
	v_mbcnt_lo_u32_b32 v0, -1, 0
	v_mbcnt_hi_u32_b32 v0, -1, v0
	s_and_b32 s0, s94, 0xffffffc0
	s_nop 0
	v_ashrrev_i32_e32 v1, 31, v0
	v_add_u32_e32 v2, s0, v0
	s_movk_i32 s0, 0x44
	v_lshlrev_b32_e32 v5, 7, v0
	v_mul_lo_u32 v4, v0, s0
	v_mul_lo_u32 v12, v2, s0
	v_lshrrev_b32_e32 v3, 1, v2
	v_and_b32_e32 v5, 0x80, v5
	s_movk_i32 s0, 0x7f
	v_and_or_b32 v3, v3, s0, v5
	s_lshl_b32 s6, s95, 3
	s_add_u32 s7, s88, 0x22000000
	s_addc_u32 s11, s89, 0
	v_add_u32_e32 v4, 0, v4
	s_add_u32 s12, s88, 0x2000000
	v_add_u32_e32 v4, s6, v4
	s_mov_b32 s1, 0
	s_addc_u32 s13, s89, 0
	s_lshl_b32 s14, s22, 5
	s_lshl_b32 s16, s22, 4
	s_lshl_b32 s10, s22, 9
	s_mov_b32 s19, 0xc3e00000
	s_movk_i32 s20, 0xff
	v_add_u32_e32 v5, 0x1100, v4
	v_add_u32_e32 v6, 0x2200, v4
	v_add_u32_e32 v7, 0x3300, v4
	v_add_u32_e32 v8, 0x4400, v4
	v_add_u32_e32 v9, 0x5500, v4
	v_add_u32_e32 v10, 0x6600, v4
	v_add_u32_e32 v11, 0x7700, v4
	v_add_u32_e32 v12, 0, v12
	s_movk_i32 s21, 0xff00
	v_mov_b32_e32 v13, 0x43e00000
	v_mov_b32_e32 v14, 8
	s_branch .LBB0_56

.LBB0_180:
	v_readlane_b32 s2, v254, 0
	v_readlane_b32 s3, v254, 1
	s_load_dwordx2 s[2:3], s[2:3], 0xd8
	s_waitcnt lgkmcnt(0)
	s_cmp_lt_i32 s2, 3
	s_cselect_b64 s[2:3], -1, 0
	s_add_u32 s4, s88, 0x3e600000
	s_addc_u32 s5, s89, 0
	v_writelane_b32 v254, s4, 47
	s_and_b64 s[0:1], s[2:3], s[0:1]
	s_andn2_b64 vcc, exec, s[0:1]
	v_writelane_b32 v254, s5, 48
	s_cbranch_vccnz .LBB0_197
	v_mbcnt_lo_u32_b32 v0, -1, 0
	v_mbcnt_hi_u32_b32 v128, -1, v0
	v_mov_b32_e32 v0, v128
	s_cmpk_gt_i32 s96, 0xc5
	s_cbranch_scc1 .LBB0_197
	s_add_u32 s33, s88, 0x400000
	s_addc_u32 s34, s89, 0
	s_add_u32 s35, s88, 0x82300000
	s_addc_u32 s36, s89, 0
	s_lshl_b32 s3, s95, 10
	v_lshlrev_b32_e32 v1, 4, v0
	v_add_u32_e32 v2, s3, v1
	v_ashrrev_i32_e32 v3, 31, v2
	v_lshrrev_b32_e32 v3, 22, v3
	v_add_u32_e32 v3, v2, v3
	v_ashrrev_i32_e32 v3, 10, v3
	v_mul_i32_i24_e32 v4, 0x400, v3
	s_add_i32 s37, s3, 0
	s_mul_hi_i32 s3, s96, 0x2aaaaaab
	v_sub_u32_e32 v2, v2, v4
	s_lshr_b32 s4, s3, 31
	v_lshrrev_b32_e32 v4, 4, v2
	s_add_i32 s20, s3, s4
	v_bitop3_b32 v2, v4, v2, 32 bitop3:0x6c
	s_mul_i32 s3, s20, -6
	s_ashr_i32 s21, s20, 31
	s_lshr_b32 s2, s94, 8
	v_ashrrev_i32_e32 v5, 31, v2
	s_add_i32 s4, s3, s96
	s_lshl_b64 s[6:7], s[20:21], 18
	v_lshrrev_b32_e32 v5, 26, v5
	s_add_u32 s24, s35, s6
	v_add_u32_e32 v5, v2, v5
	s_addc_u32 s25, s36, s7
	s_ashr_i32 s5, s4, 31
	v_lshrrev_b32_e32 v6, 6, v5
	v_and_b32_e32 v5, 0xc0, v5
	s_lshl_b64 s[6:7], s[4:5], 18
	v_lshlrev_b32_e32 v4, 3, v3
	v_lshlrev_b32_e32 v3, 5, v3
	v_sub_u32_e32 v2, v2, v5
	v_mov_b32_e32 v5, 1
	s_add_u32 s22, s33, s6
	v_and_b32_e32 v4, 0x3ffff0, v4
	v_and_b32_e32 v3, 32, v3
	v_ashrrev_i16_sdwa v2, v5, sext(v2) dst_sel:DWORD dst_unused:UNUSED_PAD src0_sel:DWORD src1_sel:BYTE_0
	s_addc_u32 s23, s34, s7
	s_add_i32 s21, s37, 0x10000
	v_add_u32_sdwa v2, v3, sext(v2) dst_sel:DWORD dst_unused:UNUSED_PAD src0_sel:DWORD src1_sel:WORD_0
	v_add_lshl_u32 v3, v6, v4, 10
	s_add_u32 s6, s22, 0x10000
	v_lshl_add_u32 v129, v2, 1, v3
	s_mov_b32 s3, m0
	s_mov_b32 m0, s21
	s_nop 0
	global_load_lds_dwordx4 v129, s[22:23]
	s_mov_b32 m0, s3
	s_addc_u32 s7, s23, 0
	s_add_i32 s38, s37, 0x12000
	s_mov_b32 s3, m0
	s_mov_b32 m0, s38
	s_nop 0
	global_load_lds_dwordx4 v129, s[6:7]
	s_mov_b32 m0, s3
	s_add_u32 s6, s22, 0x20000
	s_addc_u32 s7, s23, 0
	s_add_i32 s39, s37, 0x14000
	s_mov_b32 s3, m0
	s_mov_b32 m0, s39
	s_nop 0
	global_load_lds_dwordx4 v129, s[6:7]
	s_mov_b32 m0, s3
	s_add_u32 s6, s22, 0x30000
	s_addc_u32 s7, s23, 0
	s_add_i32 s40, s37, 0x16000
	s_mov_b32 s3, m0
	s_mov_b32 m0, s40
	s_nop 0
	global_load_lds_dwordx4 v129, s[6:7]
	s_mov_b32 m0, s3
	s_add_u32 s6, s24, 0x10000
	s_mov_b32 s3, m0
	s_mov_b32 m0, s37
	s_nop 0
	global_load_lds_dwordx4 v129, s[24:25]
	s_mov_b32 m0, s3
	s_addc_u32 s7, s25, 0
	s_add_i32 s41, s37, 0x2000
	s_mov_b32 s3, m0
	s_mov_b32 m0, s41
	s_nop 0
	global_load_lds_dwordx4 v129, s[6:7]
	s_mov_b32 m0, s3
	s_add_u32 s6, s24, 0x20000
	s_addc_u32 s7, s25, 0
	s_add_i32 s42, s37, 0x4000
	s_mov_b32 s3, m0
	s_mov_b32 m0, s42
	s_nop 0
	global_load_lds_dwordx4 v129, s[6:7]
	s_mov_b32 m0, s3
	s_add_u32 s8, s24, 0x30000
	s_addc_u32 s9, s25, 0
	s_add_i32 s43, s37, 0x6000
	s_mov_b32 s3, m0
	s_mov_b32 m0, s43
	s_nop 0
	global_load_lds_dwordx4 v129, s[8:9]
	s_mov_b32 m0, s3
	s_cmp_eq_u32 s2, 1
	s_cselect_b64 s[6:7], -1, 0
	s_cmp_lg_u32 s2, 1
	s_cbranch_scc1 .LBB0_184
	s_barrier

.LBB0_187:
	v_readlane_b32 s14, v254, 0
	v_readlane_b32 s15, v254, 1
	s_load_dword s5, s[14:15], 0xe8
	s_add_i32 s46, s46, 1
	s_waitcnt lgkmcnt(0)
	s_mul_i32 s5, s46, 0xc6
	s_add_i32 s5, s5, s96
	s_cmpk_lt_i32 s5, 0x318
	s_cselect_b64 s[16:17], -1, 0
	s_cmpk_gt_i32 s5, 0x317
	s_cbranch_scc1 .LBB0_189
	s_mul_hi_i32 s10, s5, 0x2aaaaaab
	s_lshr_b32 s11, s10, 31
	s_add_i32 s10, s10, s11
	s_mul_i32 s11, s10, -6
	s_add_i32 s12, s11, s5

.LBB0_197:
	s_cmp_lt_u32 s96, 198
	s_cbranch_scc1 .Ltc_skip_1
	v_writelane_b32 v200, s0, 0
	s_nop 1
	v_writelane_b32 v200, s1, 1
	s_nop 1
	v_writelane_b32 v200, s2, 2
	s_nop 1
	v_writelane_b32 v200, s3, 3
	s_nop 1
	v_writelane_b32 v200, s4, 4
	s_nop 1
	v_writelane_b32 v200, s5, 5
	s_nop 1
	v_writelane_b32 v200, s6, 6
	s_nop 1
	v_writelane_b32 v200, s7, 7
	s_nop 1
	v_writelane_b32 v200, s10, 8
	s_nop 1
	v_writelane_b32 v200, s11, 9
	s_nop 1
	v_writelane_b32 v200, s12, 10
	s_nop 1
	v_writelane_b32 v200, s13, 11
	s_nop 1
	v_writelane_b32 v200, s14, 12
	s_nop 1
	v_writelane_b32 v200, s15, 13
	s_nop 1
	v_writelane_b32 v200, s16, 14
	s_nop 1
	v_writelane_b32 v200, s17, 15
	s_nop 1
	v_writelane_b32 v200, s18, 16
	s_nop 1
	v_writelane_b32 v200, s19, 17
	s_nop 1
	v_writelane_b32 v200, s20, 18
	s_nop 1
	v_writelane_b32 v200, s21, 19
	s_nop 1
	v_writelane_b32 v200, s22, 20
	s_nop 1
	v_writelane_b32 v200, s23, 21
	s_nop 1
	v_writelane_b32 v200, s24, 22
	s_nop 1
	v_writelane_b32 v200, s25, 23
	s_nop 1
	v_writelane_b32 v200, s36, 24
	s_nop 1
	v_writelane_b32 v200, s37, 25
	s_nop 1
	v_writelane_b32 v200, s38, 26
	s_nop 1
	v_writelane_b32 v200, s39, 27
	s_nop 1
	v_writelane_b32 v200, s40, 28
	s_nop 1
	v_writelane_b32 v200, s41, 29
	s_nop 1
	v_writelane_b32 v200, s42, 30
	s_nop 1
	v_writelane_b32 v200, s43, 31
	s_nop 1
	v_writelane_b32 v200, s44, 32
	s_nop 1
	v_writelane_b32 v200, s45, 33
	s_nop 1
	v_writelane_b32 v200, s46, 34
	s_nop 1
	v_writelane_b32 v200, s47, 35
	s_nop 1
	v_writelane_b32 v200, s48, 36
	s_nop 1
	v_writelane_b32 v200, s49, 37
	s_nop 1
	v_writelane_b32 v200, s50, 38
	s_nop 1
	v_writelane_b32 v200, s51, 39
	s_nop 1
	s_mov_b32 s99, 1
	s_mov_b32 s98, 11
	s_mov_b32 s101, 58
	s_sub_i32 s100, s96, 198
	s_branch .Ltc_next

.LBB0_284:
	s_cmp_lt_u32 s96, 64
	s_cbranch_scc1 .Ltc_skip_2
	v_writelane_b32 v200, s0, 0
	s_nop 1
	v_writelane_b32 v200, s1, 1
	s_nop 1
	v_writelane_b32 v200, s2, 2
	s_nop 1
	v_writelane_b32 v200, s3, 3
	s_nop 1
	v_writelane_b32 v200, s4, 4
	s_nop 1
	v_writelane_b32 v200, s5, 5
	s_nop 1
	v_writelane_b32 v200, s6, 6
	s_nop 1
	v_writelane_b32 v200, s7, 7
	s_nop 1
	v_writelane_b32 v200, s10, 8
	s_nop 1
	v_writelane_b32 v200, s11, 9
	s_nop 1
	v_writelane_b32 v200, s12, 10
	s_nop 1
	v_writelane_b32 v200, s13, 11
	s_nop 1
	v_writelane_b32 v200, s14, 12
	s_nop 1
	v_writelane_b32 v200, s15, 13
	s_nop 1
	v_writelane_b32 v200, s16, 14
	s_nop 1
	v_writelane_b32 v200, s17, 15
	s_nop 1
	v_writelane_b32 v200, s18, 16
	s_nop 1
	v_writelane_b32 v200, s19, 17
	s_nop 1
	v_writelane_b32 v200, s20, 18
	s_nop 1
	v_writelane_b32 v200, s21, 19
	s_nop 1
	v_writelane_b32 v200, s22, 20
	s_nop 1
	v_writelane_b32 v200, s23, 21
	s_nop 1
	v_writelane_b32 v200, s24, 22
	s_nop 1
	v_writelane_b32 v200, s25, 23
	s_nop 1
	v_writelane_b32 v200, s36, 24
	s_nop 1
	v_writelane_b32 v200, s37, 25
	s_nop 1
	v_writelane_b32 v200, s38, 26
	s_nop 1
	v_writelane_b32 v200, s39, 27
	s_nop 1
	v_writelane_b32 v200, s40, 28
	s_nop 1
	v_writelane_b32 v200, s41, 29
	s_nop 1
	v_writelane_b32 v200, s42, 30
	s_nop 1
	v_writelane_b32 v200, s43, 31
	s_nop 1
	v_writelane_b32 v200, s44, 32
	s_nop 1
	v_writelane_b32 v200, s45, 33
	s_nop 1
	v_writelane_b32 v200, s46, 34
	s_nop 1
	v_writelane_b32 v200, s47, 35
	s_nop 1
	v_writelane_b32 v200, s48, 36
	s_nop 1
	v_writelane_b32 v200, s49, 37
	s_nop 1
	v_writelane_b32 v200, s50, 38
	s_nop 1
	v_writelane_b32 v200, s51, 39
	s_nop 1
	s_mov_b32 s99, 2
	s_mov_b32 s98, 1
	s_mov_b32 s101, 192
	s_add_i32 s100, s96, 574
	s_branch .Ltc_next

.LBB0_340:
	v_readlane_b32 s0, v254, 0
	v_readlane_b32 s1, v254, 1
	s_load_dwordx2 s[0:1], s[0:1], 0xd8
	s_waitcnt lgkmcnt(0)
	s_cmp_lt_i32 s0, 5
	s_cselect_b64 s[0:1], -1, 0
	s_and_b64 s[0:1], s[0:1], s[2:3]
	s_andn2_b64 vcc, exec, s[0:1]
	s_cbranch_vccnz .LBB0_359
	v_mbcnt_lo_u32_b32 v0, -1, 0
	v_mbcnt_hi_u32_b32 v200, -1, v0
	v_mov_b32_e32 v0, v200
	s_cmpk_gt_i32 s96, 0xaf
	s_cbranch_scc1 .LBB0_359
	s_add_u32 s30, s88, 0xa00000
	s_addc_u32 s31, s89, 0
	s_lshl_b32 s2, s95, 10
	v_lshl_add_u32 v1, v0, 4, s2
	v_ashrrev_i32_e32 v2, 31, v1
	v_lshrrev_b32_e32 v2, 22, v2
	v_add_u32_e32 v2, v1, v2
	v_ashrrev_i32_e32 v2, 10, v2
	v_mul_i32_i24_e32 v3, 0x400, v2
	v_sub_u32_e32 v1, v1, v3
	v_lshrrev_b32_e32 v3, 4, v1
	v_bitop3_b32 v1, v3, v1, 32 bitop3:0x6c
	v_ashrrev_i32_e32 v4, 31, v1
	s_add_i32 s33, s2, 0
	s_ashr_i32 s2, s96, 31
	v_lshrrev_b32_e32 v4, 26, v4
	s_lshr_b32 s2, s2, 30
	v_lshlrev_b32_e32 v3, 3, v2
	v_add_u32_e32 v4, v1, v4
	s_add_i32 s2, s96, s2
	v_and_b32_e32 v3, -16, v3
	v_ashrrev_i32_e32 v5, 6, v4
	s_ashr_i32 s16, s2, 2
	v_add_u32_e32 v3, v5, v3
	v_and_b32_e32 v5, 3, v5
	s_mov_b32 s3, 0x3fffe0
	s_and_b32 s2, s2, -4
	s_ashr_i32 s17, s16, 31
	s_lshr_b32 s4, s94, 8
	v_and_b32_e32 v4, 0xc0, v4
	v_and_or_b32 v5, v3, s3, v5
	s_sub_i32 s18, s96, s2
	s_lshl_b64 s[2:3], s[16:17], 18
	v_readlane_b32 s6, v254, 49
	v_sub_u32_e32 v1, v1, v4
	v_mov_b32_e32 v4, 1
	v_readlane_b32 s7, v254, 50
	s_add_u32 s22, s6, s2
	v_lshlrev_b32_e32 v2, 5, v2
	v_ashrrev_i16_sdwa v1, v4, sext(v1) dst_sel:DWORD dst_unused:UNUSED_PAD src0_sel:DWORD src1_sel:BYTE_0
	v_lshlrev_b32_e32 v4, 1, v3
	v_lshrrev_b32_e32 v6, 2, v3
	s_addc_u32 s23, s7, s3
	s_ashr_i32 s19, s18, 31
	v_and_b32_e32 v2, 32, v2
	v_bfe_i32 v1, v1, 0, 16
	v_and_b32_e32 v4, 24, v4
	v_and_b32_e32 v6, 4, v6
	s_lshl_b64 s[2:3], s[18:19], 18
	v_or3_b32 v4, v5, v6, v4
	v_add_lshl_u32 v1, v2, v1, 1
	s_add_u32 s20, s30, s2
	v_lshl_add_u32 v201, v4, 10, v1
	s_addc_u32 s21, s31, s3
	s_add_i32 s17, s33, 0x10000
	s_mov_b32 s2, m0
	s_mov_b32 m0, s17
	s_nop 0
	global_load_lds_dwordx4 v201, s[20:21]
	s_mov_b32 m0, s2
	s_add_u32 s2, s20, 0x10000
	s_addc_u32 s3, s21, 0
	s_add_i32 s19, s33, 0x12000
	s_mov_b32 s5, m0
	s_mov_b32 m0, s19
	s_nop 0
	global_load_lds_dwordx4 v201, s[2:3]
	s_mov_b32 m0, s5
	s_add_u32 s2, s20, 0x20000
	s_addc_u32 s3, s21, 0
	s_add_i32 s34, s33, 0x14000
	s_mov_b32 s5, m0
	s_mov_b32 m0, s34
	s_nop 0
	global_load_lds_dwordx4 v201, s[2:3]
	s_mov_b32 m0, s5
	s_add_u32 s2, s20, 0x30000
	s_addc_u32 s3, s21, 0
	s_add_i32 s35, s33, 0x16000
	s_mov_b32 s5, m0
	s_mov_b32 m0, s35
	s_nop 0
	global_load_lds_dwordx4 v201, s[2:3]
	s_mov_b32 m0, s5
	v_lshl_add_u32 v202, v3, 10, v1
	s_mov_b32 s2, m0
	s_mov_b32 m0, s33
	s_nop 0
	global_load_lds_dwordx4 v202, s[22:23]
	s_mov_b32 m0, s2
	s_add_u32 s2, s22, 0x10000
	s_addc_u32 s3, s23, 0
	s_add_i32 s36, s33, 0x2000
	s_mov_b32 s5, m0
	s_mov_b32 m0, s36
	s_nop 0
	global_load_lds_dwordx4 v202, s[2:3]
	s_mov_b32 m0, s5
	s_add_u32 s2, s22, 0x20000
	s_addc_u32 s3, s23, 0
	s_add_i32 s37, s33, 0x4000
	s_mov_b32 s5, m0
	s_mov_b32 m0, s37
	s_nop 0
	global_load_lds_dwordx4 v202, s[2:3]
	s_mov_b32 m0, s5
	s_add_u32 s6, s22, 0x30000
	s_addc_u32 s7, s23, 0
	s_add_i32 s38, s33, 0x6000
	s_mov_b32 s5, m0
	s_mov_b32 m0, s38
	s_nop 0
	global_load_lds_dwordx4 v202, s[6:7]
	s_mov_b32 m0, s5
	s_cmp_eq_u32 s4, 1
	s_cselect_b64 s[2:3], -1, 0
	s_cmp_lg_u32 s4, 1
	s_cbranch_scc1 .LBB0_344
	s_barrier

.LBB0_347:
	v_readlane_b32 s10, v254, 0
	v_readlane_b32 s11, v254, 1
	s_load_dword s7, s[10:11], 0xe8
	s_add_i32 s43, s43, 1
	s_waitcnt lgkmcnt(0)
	s_mul_i32 s7, s43, 0xb0
	s_add_i32 s7, s7, s96
	s_cmpk_lt_i32 s7, 0x210
	s_cselect_b64 s[12:13], -1, 0
	s_cmpk_gt_i32 s7, 0x20f
	s_cbranch_scc1 .LBB0_349
	s_ashr_i32 s6, s7, 31
	s_lshr_b32 s6, s6, 30
	s_add_i32 s8, s7, s6
	s_ashr_i32 s6, s8, 2
	s_and_b32 s8, s8, -4
	s_sub_i32 s8, s7, s8

.LBB0_359:
	s_cmp_lt_u32 s96, 176
	s_cbranch_scc1 .Ltc_skip_3
	v_writelane_b32 v200, s0, 0
	s_nop 1
	v_writelane_b32 v200, s1, 1
	s_nop 1
	v_writelane_b32 v200, s2, 2
	s_nop 1
	v_writelane_b32 v200, s3, 3
	s_nop 1
	v_writelane_b32 v200, s4, 4
	s_nop 1
	v_writelane_b32 v200, s5, 5
	s_nop 1
	v_writelane_b32 v200, s6, 6
	s_nop 1
	v_writelane_b32 v200, s7, 7
	s_nop 1
	v_writelane_b32 v200, s10, 8
	s_nop 1
	v_writelane_b32 v200, s11, 9
	s_nop 1
	v_writelane_b32 v200, s12, 10
	s_nop 1
	v_writelane_b32 v200, s13, 11
	s_nop 1
	v_writelane_b32 v200, s14, 12
	s_nop 1
	v_writelane_b32 v200, s15, 13
	s_nop 1
	v_writelane_b32 v200, s16, 14
	s_nop 1
	v_writelane_b32 v200, s17, 15
	s_nop 1
	v_writelane_b32 v200, s18, 16
	s_nop 1
	v_writelane_b32 v200, s19, 17
	s_nop 1
	v_writelane_b32 v200, s20, 18
	s_nop 1
	v_writelane_b32 v200, s21, 19
	s_nop 1
	v_writelane_b32 v200, s22, 20
	s_nop 1
	v_writelane_b32 v200, s23, 21
	s_nop 1
	v_writelane_b32 v200, s24, 22
	s_nop 1
	v_writelane_b32 v200, s25, 23
	s_nop 1
	v_writelane_b32 v200, s36, 24
	s_nop 1
	v_writelane_b32 v200, s37, 25
	s_nop 1
	v_writelane_b32 v200, s38, 26
	s_nop 1
	v_writelane_b32 v200, s39, 27
	s_nop 1
	v_writelane_b32 v200, s40, 28
	s_nop 1
	v_writelane_b32 v200, s41, 29
	s_nop 1
	v_writelane_b32 v200, s42, 30
	s_nop 1
	v_writelane_b32 v200, s43, 31
	s_nop 1
	v_writelane_b32 v200, s44, 32
	s_nop 1
	v_writelane_b32 v200, s45, 33
	s_nop 1
	v_writelane_b32 v200, s46, 34
	s_nop 1
	v_writelane_b32 v200, s47, 35
	s_nop 1
	v_writelane_b32 v200, s48, 36
	s_nop 1
	v_writelane_b32 v200, s49, 37
	s_nop 1
	v_writelane_b32 v200, s50, 38
	s_nop 1
	v_writelane_b32 v200, s51, 39
	s_nop 1
	s_mov_b32 s99, 3
	s_mov_b32 s98, 6
	s_mov_b32 s101, 80
	s_add_i32 s100, s96, 654
	s_branch .Ltc_next

.LBB0_668:
	s_cmp_lt_u32 s96, 144
	s_cbranch_scc1 .Ltc_skip_4
	v_writelane_b32 v200, s0, 0
	s_nop 1
	v_writelane_b32 v200, s1, 1
	s_nop 1
	v_writelane_b32 v200, s2, 2
	s_nop 1
	v_writelane_b32 v200, s3, 3
	s_nop 1
	v_writelane_b32 v200, s4, 4
	s_nop 1
	v_writelane_b32 v200, s5, 5
	s_nop 1
	v_writelane_b32 v200, s6, 6
	s_nop 1
	v_writelane_b32 v200, s7, 7
	s_nop 1
	v_writelane_b32 v200, s10, 8
	s_nop 1
	v_writelane_b32 v200, s11, 9
	s_nop 1
	v_writelane_b32 v200, s12, 10
	s_nop 1
	v_writelane_b32 v200, s13, 11
	s_nop 1
	v_writelane_b32 v200, s14, 12
	s_nop 1
	v_writelane_b32 v200, s15, 13
	s_nop 1
	v_writelane_b32 v200, s16, 14
	s_nop 1
	v_writelane_b32 v200, s17, 15
	s_nop 1
	v_writelane_b32 v200, s18, 16
	s_nop 1
	v_writelane_b32 v200, s19, 17
	s_nop 1
	v_writelane_b32 v200, s20, 18
	s_nop 1
	v_writelane_b32 v200, s21, 19
	s_nop 1
	v_writelane_b32 v200, s22, 20
	s_nop 1
	v_writelane_b32 v200, s23, 21
	s_nop 1
	v_writelane_b32 v200, s24, 22
	s_nop 1
	v_writelane_b32 v200, s25, 23
	s_nop 1
	v_writelane_b32 v200, s36, 24
	s_nop 1
	v_writelane_b32 v200, s37, 25
	s_nop 1
	v_writelane_b32 v200, s38, 26
	s_nop 1
	v_writelane_b32 v200, s39, 27
	s_nop 1
	v_writelane_b32 v200, s40, 28
	s_nop 1
	v_writelane_b32 v200, s41, 29
	s_nop 1
	v_writelane_b32 v200, s42, 30
	s_nop 1
	v_writelane_b32 v200, s43, 31
	s_nop 1
	v_writelane_b32 v200, s44, 32
	s_nop 1
	v_writelane_b32 v200, s45, 33
	s_nop 1
	v_writelane_b32 v200, s46, 34
	s_nop 1
	v_writelane_b32 v200, s47, 35
	s_nop 1
	v_writelane_b32 v200, s48, 36
	s_nop 1
	v_writelane_b32 v200, s49, 37
	s_nop 1
	v_writelane_b32 v200, s50, 38
	s_nop 1
	v_writelane_b32 v200, s51, 39
	s_nop 1
	s_mov_b32 s99, 4
	s_mov_b32 s98, 2
	s_mov_b32 s101, 112
	s_add_i32 s100, s96, 1166
	s_branch .Ltc_next

.LBB0_790:
	v_readlane_b32 s0, v254, 0
	v_readlane_b32 s1, v254, 1
	s_load_dwordx2 s[0:1], s[0:1], 0xd8
	s_waitcnt lgkmcnt(0)
	s_cmp_lt_i32 s0, 10
	s_cselect_b64 s[0:1], -1, 0
	s_and_b64 s[0:1], s[0:1], s[2:3]
	s_andn2_b64 vcc, exec, s[0:1]
	s_cbranch_vccnz .LBB0_807
	v_mbcnt_lo_u32_b32 v0, -1, 0
	v_mbcnt_hi_u32_b32 v132, -1, v0
	v_mov_b32_e32 v0, v132
	s_cmpk_gt_i32 s96, 0xe2
	s_cbranch_scc1 .LBB0_807
	s_add_u32 s30, s88, 0xe00000
	s_addc_u32 s31, s89, 0
	s_add_u32 s33, s88, 0x82300000
	s_addc_u32 s34, s89, 0
	s_lshl_b32 s2, s95, 10
	v_lshl_add_u32 v1, v0, 4, s2
	v_ashrrev_i32_e32 v2, 31, v1
	v_lshrrev_b32_e32 v2, 22, v2
	v_add_u32_e32 v2, v1, v2
	v_ashrrev_i32_e32 v2, 10, v2
	v_mul_i32_i24_e32 v3, 0x400, v2
	v_sub_u32_e32 v1, v1, v3
	v_lshrrev_b32_e32 v3, 4, v1
	v_bitop3_b32 v1, v3, v1, 32 bitop3:0x6c
	v_ashrrev_i32_e32 v4, 31, v1
	v_lshrrev_b32_e32 v4, 26, v4
	v_lshlrev_b32_e32 v3, 3, v2
	v_add_u32_e32 v4, v1, v4
	v_and_b32_e32 v3, -16, v3
	v_ashrrev_i32_e32 v5, 6, v4
	v_add_u32_e32 v3, v5, v3
	v_and_b32_e32 v5, 3, v5
	s_mov_b32 s3, 0x3fffe0
	s_add_i32 s35, s2, 0
	s_mul_hi_i32 s2, s96, 0x2aaaaaab
	v_and_or_b32 v5, v3, s3, v5
	s_lshr_b32 s3, s2, 31
	s_ashr_i32 s2, s2, 1
	s_add_i32 s18, s2, s3
	s_mul_i32 s2, s18, -12
	s_ashr_i32 s19, s18, 31
	s_lshr_b32 s4, s94, 8
	v_and_b32_e32 v4, 0xc0, v4
	s_add_i32 s16, s2, s96
	s_lshl_b64 s[2:3], s[18:19], 18
	v_sub_u32_e32 v1, v1, v4
	v_mov_b32_e32 v4, 1
	s_add_u32 s22, s33, s2
	v_lshlrev_b32_e32 v2, 5, v2
	v_ashrrev_i16_sdwa v1, v4, sext(v1) dst_sel:DWORD dst_unused:UNUSED_PAD src0_sel:DWORD src1_sel:BYTE_0
	v_lshlrev_b32_e32 v4, 1, v3
	v_lshrrev_b32_e32 v6, 2, v3
	s_addc_u32 s23, s34, s3
	s_ashr_i32 s17, s16, 31
	v_and_b32_e32 v2, 32, v2
	v_bfe_i32 v1, v1, 0, 16
	v_and_b32_e32 v4, 24, v4
	v_and_b32_e32 v6, 4, v6
	s_lshl_b64 s[2:3], s[16:17], 18
	v_or3_b32 v4, v5, v6, v4
	v_add_lshl_u32 v1, v2, v1, 1
	s_add_u32 s20, s30, s2
	v_lshl_add_u32 v133, v4, 10, v1
	s_addc_u32 s21, s31, s3
	s_add_i32 s17, s35, 0x10000
	s_mov_b32 s2, m0
	s_mov_b32 m0, s17
	s_nop 0
	global_load_lds_dwordx4 v133, s[20:21]
	s_mov_b32 m0, s2
	s_add_u32 s2, s20, 0x10000
	s_addc_u32 s3, s21, 0
	s_add_i32 s19, s35, 0x12000
	s_mov_b32 s5, m0
	s_mov_b32 m0, s19
	s_nop 0
	global_load_lds_dwordx4 v133, s[2:3]
	s_mov_b32 m0, s5
	s_add_u32 s2, s20, 0x20000
	s_addc_u32 s3, s21, 0
	s_add_i32 s36, s35, 0x14000
	s_mov_b32 s5, m0
	s_mov_b32 m0, s36
	s_nop 0
	global_load_lds_dwordx4 v133, s[2:3]
	s_mov_b32 m0, s5
	s_add_u32 s2, s20, 0x30000
	s_addc_u32 s3, s21, 0
	s_add_i32 s37, s35, 0x16000
	s_mov_b32 s5, m0
	s_mov_b32 m0, s37
	s_nop 0
	global_load_lds_dwordx4 v133, s[2:3]
	s_mov_b32 m0, s5
	v_lshl_add_u32 v134, v3, 10, v1
	s_mov_b32 s2, m0
	s_mov_b32 m0, s35
	s_nop 0
	global_load_lds_dwordx4 v134, s[22:23]
	s_mov_b32 m0, s2
	s_add_u32 s2, s22, 0x10000
	s_addc_u32 s3, s23, 0
	s_add_i32 s38, s35, 0x2000
	s_mov_b32 s5, m0
	s_mov_b32 m0, s38
	s_nop 0
	global_load_lds_dwordx4 v134, s[2:3]
	s_mov_b32 m0, s5
	s_add_u32 s2, s22, 0x20000
	s_addc_u32 s3, s23, 0
	s_add_i32 s39, s35, 0x4000
	s_mov_b32 s5, m0
	s_mov_b32 m0, s39
	s_nop 0
	global_load_lds_dwordx4 v134, s[2:3]
	s_mov_b32 m0, s5
	s_add_u32 s6, s22, 0x30000
	s_addc_u32 s7, s23, 0
	s_add_i32 s40, s35, 0x6000
	s_mov_b32 s5, m0
	s_mov_b32 m0, s40
	s_nop 0
	global_load_lds_dwordx4 v134, s[6:7]
	s_mov_b32 m0, s5
	s_cmp_eq_u32 s4, 1
	s_cselect_b64 s[2:3], -1, 0
	s_cmp_lg_u32 s4, 1
	s_cbranch_scc1 .LBB0_794
	s_barrier

.LBB0_797:
	v_readlane_b32 s10, v254, 0
	v_readlane_b32 s11, v254, 1
	s_load_dword s7, s[10:11], 0xe8
	s_add_i32 s43, s43, 1
	s_waitcnt lgkmcnt(0)
	s_mul_i32 s7, s43, 0xe3
	s_add_i32 s7, s7, s96
	s_cmpk_lt_i32 s7, 0x630
	s_cselect_b64 s[12:13], -1, 0
	s_cmpk_gt_i32 s7, 0x62f
	s_cbranch_scc1 .LBB0_799
	s_mul_hi_i32 s6, s7, 0x2aaaaaab
	s_lshr_b32 s8, s6, 31
	s_ashr_i32 s6, s6, 1
	s_add_i32 s6, s6, s8
	s_mul_i32 s8, s6, -12
	s_add_i32 s8, s8, s7

.LBB0_807:
	s_cmp_lt_u32 s96, 227
	s_cbranch_scc1 .Ltc_skip_5
	v_writelane_b32 v200, s0, 0
	s_nop 1
	v_writelane_b32 v200, s1, 1
	s_nop 1
	v_writelane_b32 v200, s2, 2
	s_nop 1
	v_writelane_b32 v200, s3, 3
	s_nop 1
	v_writelane_b32 v200, s4, 4
	s_nop 1
	v_writelane_b32 v200, s5, 5
	s_nop 1
	v_writelane_b32 v200, s6, 6
	s_nop 1
	v_writelane_b32 v200, s7, 7
	s_nop 1
	v_writelane_b32 v200, s10, 8
	s_nop 1
	v_writelane_b32 v200, s11, 9
	s_nop 1
	v_writelane_b32 v200, s12, 10
	s_nop 1
	v_writelane_b32 v200, s13, 11
	s_nop 1
	v_writelane_b32 v200, s14, 12
	s_nop 1
	v_writelane_b32 v200, s15, 13
	s_nop 1
	v_writelane_b32 v200, s16, 14
	s_nop 1
	v_writelane_b32 v200, s17, 15
	s_nop 1
	v_writelane_b32 v200, s18, 16
	s_nop 1
	v_writelane_b32 v200, s19, 17
	s_nop 1
	v_writelane_b32 v200, s20, 18
	s_nop 1
	v_writelane_b32 v200, s21, 19
	s_nop 1
	v_writelane_b32 v200, s22, 20
	s_nop 1
	v_writelane_b32 v200, s23, 21
	s_nop 1
	v_writelane_b32 v200, s24, 22
	s_nop 1
	v_writelane_b32 v200, s25, 23
	s_nop 1
	v_writelane_b32 v200, s36, 24
	s_nop 1
	v_writelane_b32 v200, s37, 25
	s_nop 1
	v_writelane_b32 v200, s38, 26
	s_nop 1
	v_writelane_b32 v200, s39, 27
	s_nop 1
	v_writelane_b32 v200, s40, 28
	s_nop 1
	v_writelane_b32 v200, s41, 29
	s_nop 1
	v_writelane_b32 v200, s42, 30
	s_nop 1
	v_writelane_b32 v200, s43, 31
	s_nop 1
	v_writelane_b32 v200, s44, 32
	s_nop 1
	v_writelane_b32 v200, s45, 33
	s_nop 1
	v_writelane_b32 v200, s46, 34
	s_nop 1
	v_writelane_b32 v200, s47, 35
	s_nop 1
	v_writelane_b32 v200, s48, 36
	s_nop 1
	v_writelane_b32 v200, s49, 37
	s_nop 1
	v_writelane_b32 v200, s50, 38
	s_nop 1
	v_writelane_b32 v200, s51, 39
	s_nop 1
	s_mov_b32 s99, 5
	s_mov_b32 s98, 19
	s_mov_b32 s101, 29
	s_add_i32 s100, s96, 1307
	s_branch .Ltc_next

.LBB0_1033:
	v_readlane_b32 s0, v254, 0
	v_readlane_b32 s1, v254, 1
	s_load_dwordx2 s[0:1], s[0:1], 0xd8
	s_waitcnt lgkmcnt(0)
	s_cmp_lt_i32 s0, 13
	s_cselect_b64 s[0:1], -1, 0
	s_and_b64 s[0:1], s[0:1], s[2:3]
	s_andn2_b64 vcc, exec, s[0:1]
	s_cbranch_vccnz .LBB0_1052
	v_mbcnt_lo_u32_b32 v0, -1, 0
	v_mbcnt_hi_u32_b32 v200, -1, v0
	v_mov_b32_e32 v0, v200
	s_cmpk_gt_i32 s96, 0xaf
	s_cbranch_scc1 .LBB0_1052
	s_add_u32 s30, s88, 0x1400000
	s_addc_u32 s31, s89, 0
	s_lshl_b32 s2, s95, 10
	v_lshl_add_u32 v1, v0, 4, s2
	v_ashrrev_i32_e32 v2, 31, v1
	v_lshrrev_b32_e32 v2, 22, v2
	v_add_u32_e32 v2, v1, v2
	v_ashrrev_i32_e32 v2, 10, v2
	v_mul_i32_i24_e32 v3, 0x400, v2
	v_sub_u32_e32 v1, v1, v3
	v_lshrrev_b32_e32 v3, 4, v1
	v_bitop3_b32 v1, v3, v1, 32 bitop3:0x6c
	v_ashrrev_i32_e32 v4, 31, v1
	s_add_i32 s33, s2, 0
	s_ashr_i32 s2, s96, 31
	v_lshrrev_b32_e32 v4, 26, v4
	s_lshr_b32 s2, s2, 30
	v_lshlrev_b32_e32 v3, 3, v2
	v_add_u32_e32 v4, v1, v4
	s_add_i32 s2, s96, s2
	v_and_b32_e32 v3, -16, v3
	v_ashrrev_i32_e32 v5, 6, v4
	s_ashr_i32 s16, s2, 2
	v_add_u32_e32 v3, v5, v3
	v_and_b32_e32 v5, 3, v5
	s_mov_b32 s3, 0x3fffe0
	s_and_b32 s2, s2, -4
	s_ashr_i32 s17, s16, 31
	s_lshr_b32 s4, s94, 8
	v_and_b32_e32 v4, 0xc0, v4
	v_and_or_b32 v5, v3, s3, v5
	s_sub_i32 s18, s96, s2
	s_lshl_b64 s[2:3], s[16:17], 18
	v_readlane_b32 s6, v254, 49
	v_sub_u32_e32 v1, v1, v4
	v_mov_b32_e32 v4, 1
	v_readlane_b32 s7, v254, 50
	s_add_u32 s22, s6, s2
	v_lshlrev_b32_e32 v2, 5, v2
	v_ashrrev_i16_sdwa v1, v4, sext(v1) dst_sel:DWORD dst_unused:UNUSED_PAD src0_sel:DWORD src1_sel:BYTE_0
	v_lshlrev_b32_e32 v4, 1, v3
	v_lshrrev_b32_e32 v6, 2, v3
	s_addc_u32 s23, s7, s3
	s_ashr_i32 s19, s18, 31
	v_and_b32_e32 v2, 32, v2
	v_bfe_i32 v1, v1, 0, 16
	v_and_b32_e32 v4, 24, v4
	v_and_b32_e32 v6, 4, v6
	s_lshl_b64 s[2:3], s[18:19], 18
	v_or3_b32 v4, v5, v6, v4
	v_add_lshl_u32 v1, v2, v1, 1
	s_add_u32 s20, s30, s2
	v_lshl_add_u32 v201, v4, 10, v1
	s_addc_u32 s21, s31, s3
	s_add_i32 s17, s33, 0x10000
	s_mov_b32 s2, m0
	s_mov_b32 m0, s17
	s_nop 0
	global_load_lds_dwordx4 v201, s[20:21]
	s_mov_b32 m0, s2
	s_add_u32 s2, s20, 0x10000
	s_addc_u32 s3, s21, 0
	s_add_i32 s19, s33, 0x12000
	s_mov_b32 s5, m0
	s_mov_b32 m0, s19
	s_nop 0
	global_load_lds_dwordx4 v201, s[2:3]
	s_mov_b32 m0, s5
	s_add_u32 s2, s20, 0x20000
	s_addc_u32 s3, s21, 0
	s_add_i32 s34, s33, 0x14000
	s_mov_b32 s5, m0
	s_mov_b32 m0, s34
	s_nop 0
	global_load_lds_dwordx4 v201, s[2:3]
	s_mov_b32 m0, s5
	s_add_u32 s2, s20, 0x30000
	s_addc_u32 s3, s21, 0
	s_add_i32 s35, s33, 0x16000
	s_mov_b32 s5, m0
	s_mov_b32 m0, s35
	s_nop 0
	global_load_lds_dwordx4 v201, s[2:3]
	s_mov_b32 m0, s5
	v_lshl_add_u32 v202, v3, 10, v1
	s_mov_b32 s2, m0
	s_mov_b32 m0, s33
	s_nop 0
	global_load_lds_dwordx4 v202, s[22:23]
	s_mov_b32 m0, s2
	s_add_u32 s2, s22, 0x10000
	s_addc_u32 s3, s23, 0
	s_add_i32 s36, s33, 0x2000
	s_mov_b32 s5, m0
	s_mov_b32 m0, s36
	s_nop 0
	global_load_lds_dwordx4 v202, s[2:3]
	s_mov_b32 m0, s5
	s_add_u32 s2, s22, 0x20000
	s_addc_u32 s3, s23, 0
	s_add_i32 s37, s33, 0x4000
	s_mov_b32 s5, m0
	s_mov_b32 m0, s37
	s_nop 0
	global_load_lds_dwordx4 v202, s[2:3]
	s_mov_b32 m0, s5
	s_add_u32 s6, s22, 0x30000
	s_addc_u32 s7, s23, 0
	s_add_i32 s38, s33, 0x6000
	s_mov_b32 s5, m0
	s_mov_b32 m0, s38
	s_nop 0
	global_load_lds_dwordx4 v202, s[6:7]
	s_mov_b32 m0, s5
	s_cmp_eq_u32 s4, 1
	s_cselect_b64 s[2:3], -1, 0
	s_cmp_lg_u32 s4, 1
	s_cbranch_scc1 .LBB0_1037
	s_barrier

.LBB0_1052:
	s_cmp_lt_u32 s96, 176
	s_cbranch_scc1 .Ltc_skip_6
	v_writelane_b32 v200, s0, 0
	s_nop 1
	v_writelane_b32 v200, s1, 1
	s_nop 1
	v_writelane_b32 v200, s2, 2
	s_nop 1
	v_writelane_b32 v200, s3, 3
	s_nop 1
	v_writelane_b32 v200, s4, 4
	s_nop 1
	v_writelane_b32 v200, s5, 5
	s_nop 1
	v_writelane_b32 v200, s6, 6
	s_nop 1
	v_writelane_b32 v200, s7, 7
	s_nop 1
	v_writelane_b32 v200, s10, 8
	s_nop 1
	v_writelane_b32 v200, s11, 9
	s_nop 1
	v_writelane_b32 v200, s12, 10
	s_nop 1
	v_writelane_b32 v200, s13, 11
	s_nop 1
	v_writelane_b32 v200, s14, 12
	s_nop 1
	v_writelane_b32 v200, s15, 13
	s_nop 1
	v_writelane_b32 v200, s16, 14
	s_nop 1
	v_writelane_b32 v200, s17, 15
	s_nop 1
	v_writelane_b32 v200, s18, 16
	s_nop 1
	v_writelane_b32 v200, s19, 17
	s_nop 1
	v_writelane_b32 v200, s20, 18
	s_nop 1
	v_writelane_b32 v200, s21, 19
	s_nop 1
	v_writelane_b32 v200, s22, 20
	s_nop 1
	v_writelane_b32 v200, s23, 21
	s_nop 1
	v_writelane_b32 v200, s24, 22
	s_nop 1
	v_writelane_b32 v200, s25, 23
	s_nop 1
	v_writelane_b32 v200, s36, 24
	s_nop 1
	v_writelane_b32 v200, s37, 25
	s_nop 1
	v_writelane_b32 v200, s38, 26
	s_nop 1
	v_writelane_b32 v200, s39, 27
	s_nop 1
	v_writelane_b32 v200, s40, 28
	s_nop 1
	v_writelane_b32 v200, s41, 29
	s_nop 1
	v_writelane_b32 v200, s42, 30
	s_nop 1
	v_writelane_b32 v200, s43, 31
	s_nop 1
	v_writelane_b32 v200, s44, 32
	s_nop 1
	v_writelane_b32 v200, s45, 33
	s_nop 1
	v_writelane_b32 v200, s46, 34
	s_nop 1
	v_writelane_b32 v200, s47, 35
	s_nop 1
	v_writelane_b32 v200, s48, 36
	s_nop 1
	v_writelane_b32 v200, s49, 37
	s_nop 1
	v_writelane_b32 v200, s50, 38
	s_nop 1
	v_writelane_b32 v200, s51, 39
	s_nop 1
	s_mov_b32 s99, 6
	s_mov_b32 s98, 6
	s_mov_b32 s101, 80
	s_add_i32 s100, s96, 1909
	s_branch .Ltc_next

.LBB0_1361:
	s_cmp_lt_u32 s96, 144
	s_cbranch_scc1 .Ltc_skip_7
	v_writelane_b32 v200, s0, 0
	s_nop 1
	v_writelane_b32 v200, s1, 1
	s_nop 1
	v_writelane_b32 v200, s2, 2
	s_nop 1
	v_writelane_b32 v200, s3, 3
	s_nop 1
	v_writelane_b32 v200, s4, 4
	s_nop 1
	v_writelane_b32 v200, s5, 5
	s_nop 1
	v_writelane_b32 v200, s6, 6
	s_nop 1
	v_writelane_b32 v200, s7, 7
	s_nop 1
	v_writelane_b32 v200, s10, 8
	s_nop 1
	v_writelane_b32 v200, s11, 9
	s_nop 1
	v_writelane_b32 v200, s12, 10
	s_nop 1
	v_writelane_b32 v200, s13, 11
	s_nop 1
	v_writelane_b32 v200, s14, 12
	s_nop 1
	v_writelane_b32 v200, s15, 13
	s_nop 1
	v_writelane_b32 v200, s16, 14
	s_nop 1
	v_writelane_b32 v200, s17, 15
	s_nop 1
	v_writelane_b32 v200, s18, 16
	s_nop 1
	v_writelane_b32 v200, s19, 17
	s_nop 1
	v_writelane_b32 v200, s20, 18
	s_nop 1
	v_writelane_b32 v200, s21, 19
	s_nop 1
	v_writelane_b32 v200, s22, 20
	s_nop 1
	v_writelane_b32 v200, s23, 21
	s_nop 1
	v_writelane_b32 v200, s24, 22
	s_nop 1
	v_writelane_b32 v200, s25, 23
	s_nop 1
	v_writelane_b32 v200, s36, 24
	s_nop 1
	v_writelane_b32 v200, s37, 25
	s_nop 1
	v_writelane_b32 v200, s38, 26
	s_nop 1
	v_writelane_b32 v200, s39, 27
	s_nop 1
	v_writelane_b32 v200, s40, 28
	s_nop 1
	v_writelane_b32 v200, s41, 29
	s_nop 1
	v_writelane_b32 v200, s42, 30
	s_nop 1
	v_writelane_b32 v200, s43, 31
	s_nop 1
	v_writelane_b32 v200, s44, 32
	s_nop 1
	v_writelane_b32 v200, s45, 33
	s_nop 1
	v_writelane_b32 v200, s46, 34
	s_nop 1
	v_writelane_b32 v200, s47, 35
	s_nop 1
	v_writelane_b32 v200, s48, 36
	s_nop 1
	v_writelane_b32 v200, s49, 37
	s_nop 1
	v_writelane_b32 v200, s50, 38
	s_nop 1
	v_writelane_b32 v200, s51, 39
	s_nop 1
	s_mov_b32 s99, 7
	s_mov_b32 s98, 2
	s_mov_b32 s101, 112
	s_add_i32 s100, s96, 2421
	s_branch .Ltc_s1_back

.LBB0_1478:
	v_readlane_b32 s0, v254, 0
	v_readlane_b32 s1, v254, 1
	s_load_dwordx2 s[0:1], s[0:1], 0xd8
	s_waitcnt lgkmcnt(0)
	s_cmp_lt_i32 s0, 18
	s_cselect_b64 s[0:1], -1, 0
	s_and_b64 s[0:1], s[0:1], s[2:3]
	s_andn2_b64 vcc, exec, s[0:1]
	s_cbranch_vccnz .LBB0_1495
	v_mbcnt_lo_u32_b32 v0, -1, 0
	v_mbcnt_hi_u32_b32 v132, -1, v0
	v_mov_b32_e32 v0, v132
	s_cmpk_gt_i32 s96, 0xe2
	s_cbranch_scc1 .LBB0_1495
	s_add_u32 s30, s88, 0x1600000
	s_addc_u32 s31, s89, 0
	s_add_u32 s33, s88, 0x82300000
	s_addc_u32 s34, s89, 0
	s_lshl_b32 s2, s95, 10
	v_lshl_add_u32 v1, v0, 4, s2
	v_ashrrev_i32_e32 v2, 31, v1
	v_lshrrev_b32_e32 v2, 22, v2
	v_add_u32_e32 v2, v1, v2
	v_ashrrev_i32_e32 v2, 10, v2
	v_mul_i32_i24_e32 v3, 0x400, v2
	v_sub_u32_e32 v1, v1, v3
	v_lshrrev_b32_e32 v3, 4, v1
	v_bitop3_b32 v1, v3, v1, 32 bitop3:0x6c
	v_ashrrev_i32_e32 v4, 31, v1
	v_lshrrev_b32_e32 v4, 26, v4
	v_lshlrev_b32_e32 v3, 3, v2
	v_add_u32_e32 v4, v1, v4
	v_and_b32_e32 v3, -16, v3
	v_ashrrev_i32_e32 v5, 6, v4
	v_add_u32_e32 v3, v5, v3
	v_and_b32_e32 v5, 3, v5
	s_mov_b32 s3, 0x3fffe0
	s_add_i32 s35, s2, 0
	s_mul_hi_i32 s2, s96, 0x2aaaaaab
	v_and_or_b32 v5, v3, s3, v5
	s_lshr_b32 s3, s2, 31
	s_ashr_i32 s2, s2, 1
	s_add_i32 s18, s2, s3
	s_mul_i32 s2, s18, -12
	s_ashr_i32 s19, s18, 31
	s_lshr_b32 s4, s94, 8
	v_and_b32_e32 v4, 0xc0, v4
	s_add_i32 s16, s2, s96
	s_lshl_b64 s[2:3], s[18:19], 18
	v_sub_u32_e32 v1, v1, v4
	v_mov_b32_e32 v4, 1
	s_add_u32 s22, s33, s2
	v_lshlrev_b32_e32 v2, 5, v2
	v_ashrrev_i16_sdwa v1, v4, sext(v1) dst_sel:DWORD dst_unused:UNUSED_PAD src0_sel:DWORD src1_sel:BYTE_0
	v_lshlrev_b32_e32 v4, 1, v3
	v_lshrrev_b32_e32 v6, 2, v3
	s_addc_u32 s23, s34, s3
	s_ashr_i32 s17, s16, 31
	v_and_b32_e32 v2, 32, v2
	v_bfe_i32 v1, v1, 0, 16
	v_and_b32_e32 v4, 24, v4
	v_and_b32_e32 v6, 4, v6
	s_lshl_b64 s[2:3], s[16:17], 18
	v_or3_b32 v4, v5, v6, v4
	v_add_lshl_u32 v1, v2, v1, 1
	s_add_u32 s20, s30, s2
	v_lshl_add_u32 v133, v4, 10, v1
	s_addc_u32 s21, s31, s3
	s_add_i32 s17, s35, 0x10000
	s_mov_b32 s2, m0
	s_mov_b32 m0, s17
	s_nop 0
	global_load_lds_dwordx4 v133, s[20:21]
	s_mov_b32 m0, s2
	s_add_u32 s2, s20, 0x10000
	s_addc_u32 s3, s21, 0
	s_add_i32 s19, s35, 0x12000
	s_mov_b32 s5, m0
	s_mov_b32 m0, s19
	s_nop 0
	global_load_lds_dwordx4 v133, s[2:3]
	s_mov_b32 m0, s5
	s_add_u32 s2, s20, 0x20000
	s_addc_u32 s3, s21, 0
	s_add_i32 s36, s35, 0x14000
	s_mov_b32 s5, m0
	s_mov_b32 m0, s36
	s_nop 0
	global_load_lds_dwordx4 v133, s[2:3]
	s_mov_b32 m0, s5
	s_add_u32 s2, s20, 0x30000
	s_addc_u32 s3, s21, 0
	s_add_i32 s37, s35, 0x16000
	s_mov_b32 s5, m0
	s_mov_b32 m0, s37
	s_nop 0
	global_load_lds_dwordx4 v133, s[2:3]
	s_mov_b32 m0, s5
	v_lshl_add_u32 v134, v3, 10, v1
	s_mov_b32 s2, m0
	s_mov_b32 m0, s35
	s_nop 0
	global_load_lds_dwordx4 v134, s[22:23]
	s_mov_b32 m0, s2
	s_add_u32 s2, s22, 0x10000
	s_addc_u32 s3, s23, 0
	s_add_i32 s38, s35, 0x2000
	s_mov_b32 s5, m0
	s_mov_b32 m0, s38
	s_nop 0
	global_load_lds_dwordx4 v134, s[2:3]
	s_mov_b32 m0, s5
	s_add_u32 s2, s22, 0x20000
	s_addc_u32 s3, s23, 0
	s_add_i32 s39, s35, 0x4000
	s_mov_b32 s5, m0
	s_mov_b32 m0, s39
	s_nop 0
	global_load_lds_dwordx4 v134, s[2:3]
	s_mov_b32 m0, s5
	s_add_u32 s6, s22, 0x30000
	s_addc_u32 s7, s23, 0
	s_add_i32 s40, s35, 0x6000
	s_mov_b32 s5, m0
	s_mov_b32 m0, s40
	s_nop 0
	global_load_lds_dwordx4 v134, s[6:7]
	s_mov_b32 m0, s5
	s_cmp_eq_u32 s4, 1
	s_cselect_b64 s[2:3], -1, 0
	s_cmp_lg_u32 s4, 1
	s_cbranch_scc1 .LBB0_1482
	s_barrier

.LBB0_1495:
	s_cmp_lt_u32 s96, 227
	s_cbranch_scc1 .Ltc_skip_8
	v_writelane_b32 v200, s0, 0
	s_nop 1
	v_writelane_b32 v200, s1, 1
	s_nop 1
	v_writelane_b32 v200, s2, 2
	s_nop 1
	v_writelane_b32 v200, s3, 3
	s_nop 1
	v_writelane_b32 v200, s4, 4
	s_nop 1
	v_writelane_b32 v200, s5, 5
	s_nop 1
	v_writelane_b32 v200, s6, 6
	s_nop 1
	v_writelane_b32 v200, s7, 7
	s_nop 1
	v_writelane_b32 v200, s10, 8
	s_nop 1
	v_writelane_b32 v200, s11, 9
	s_nop 1
	v_writelane_b32 v200, s12, 10
	s_nop 1
	v_writelane_b32 v200, s13, 11
	s_nop 1
	v_writelane_b32 v200, s14, 12
	s_nop 1
	v_writelane_b32 v200, s15, 13
	s_nop 1
	v_writelane_b32 v200, s16, 14
	s_nop 1
	v_writelane_b32 v200, s17, 15
	s_nop 1
	v_writelane_b32 v200, s18, 16
	s_nop 1
	v_writelane_b32 v200, s19, 17
	s_nop 1
	v_writelane_b32 v200, s20, 18
	s_nop 1
	v_writelane_b32 v200, s21, 19
	s_nop 1
	v_writelane_b32 v200, s22, 20
	s_nop 1
	v_writelane_b32 v200, s23, 21
	s_nop 1
	v_writelane_b32 v200, s24, 22
	s_nop 1
	v_writelane_b32 v200, s25, 23
	s_nop 1
	v_writelane_b32 v200, s36, 24
	s_nop 1
	v_writelane_b32 v200, s37, 25
	s_nop 1
	v_writelane_b32 v200, s38, 26
	s_nop 1
	v_writelane_b32 v200, s39, 27
	s_nop 1
	v_writelane_b32 v200, s40, 28
	s_nop 1
	v_writelane_b32 v200, s41, 29
	s_nop 1
	v_writelane_b32 v200, s42, 30
	s_nop 1
	v_writelane_b32 v200, s43, 31
	s_nop 1
	v_writelane_b32 v200, s44, 32
	s_nop 1
	v_writelane_b32 v200, s45, 33
	s_nop 1
	v_writelane_b32 v200, s46, 34
	s_nop 1
	v_writelane_b32 v200, s47, 35
	s_nop 1
	v_writelane_b32 v200, s48, 36
	s_nop 1
	v_writelane_b32 v200, s49, 37
	s_nop 1
	v_writelane_b32 v200, s50, 38
	s_nop 1
	v_writelane_b32 v200, s51, 39
	s_nop 1
	s_mov_b32 s99, 8
	s_mov_b32 s98, 19
	s_mov_b32 s101, 29
	s_add_i32 s100, s96, 2562
	s_branch .Ltc_s1_back

.LBB0_1636:
	s_cmp_lt_u32 s96, 64
	s_cbranch_scc1 .Ltc_skip_9
	v_writelane_b32 v200, s0, 0
	s_nop 1
	v_writelane_b32 v200, s1, 1
	s_nop 1
	v_writelane_b32 v200, s2, 2
	s_nop 1
	v_writelane_b32 v200, s3, 3
	s_nop 1
	v_writelane_b32 v200, s4, 4
	s_nop 1
	v_writelane_b32 v200, s5, 5
	s_nop 1
	v_writelane_b32 v200, s6, 6
	s_nop 1
	v_writelane_b32 v200, s7, 7
	s_nop 1
	v_writelane_b32 v200, s10, 8
	s_nop 1
	v_writelane_b32 v200, s11, 9
	s_nop 1
	v_writelane_b32 v200, s12, 10
	s_nop 1
	v_writelane_b32 v200, s13, 11
	s_nop 1
	v_writelane_b32 v200, s14, 12
	s_nop 1
	v_writelane_b32 v200, s15, 13
	s_nop 1
	v_writelane_b32 v200, s16, 14
	s_nop 1
	v_writelane_b32 v200, s17, 15
	s_nop 1
	v_writelane_b32 v200, s18, 16
	s_nop 1
	v_writelane_b32 v200, s19, 17
	s_nop 1
	v_writelane_b32 v200, s20, 18
	s_nop 1
	v_writelane_b32 v200, s21, 19
	s_nop 1
	v_writelane_b32 v200, s22, 20
	s_nop 1
	v_writelane_b32 v200, s23, 21
	s_nop 1
	v_writelane_b32 v200, s24, 22
	s_nop 1
	v_writelane_b32 v200, s25, 23
	s_nop 1
	v_writelane_b32 v200, s36, 24
	s_nop 1
	v_writelane_b32 v200, s37, 25
	s_nop 1
	v_writelane_b32 v200, s38, 26
	s_nop 1
	v_writelane_b32 v200, s39, 27
	s_nop 1
	v_writelane_b32 v200, s40, 28
	s_nop 1
	v_writelane_b32 v200, s41, 29
	s_nop 1
	v_writelane_b32 v200, s42, 30
	s_nop 1
	v_writelane_b32 v200, s43, 31
	s_nop 1
	v_writelane_b32 v200, s44, 32
	s_nop 1
	v_writelane_b32 v200, s45, 33
	s_nop 1
	v_writelane_b32 v200, s46, 34
	s_nop 1
	v_writelane_b32 v200, s47, 35
	s_nop 1
	v_writelane_b32 v200, s48, 36
	s_nop 1
	v_writelane_b32 v200, s49, 37
	s_nop 1
	v_writelane_b32 v200, s50, 38
	s_nop 1
	v_writelane_b32 v200, s51, 39
	s_nop 1
	s_mov_b32 s99, 9
	s_mov_b32 s98, 1
	s_mov_b32 s101, 192
	s_add_i32 s100, s96, 3276
	s_branch .Ltc_s1_back

.LBB0_1692:
	v_readlane_b32 s2, v254, 0
	v_readlane_b32 s3, v254, 1
	s_load_dwordx2 s[2:3], s[2:3], 0xd8
	s_waitcnt lgkmcnt(0)
	s_cmp_lt_i32 s2, 20
	s_cselect_b64 s[2:3], -1, 0
	s_and_b64 s[0:1], s[2:3], s[0:1]
	s_andn2_b64 vcc, exec, s[0:1]
	s_cbranch_vccnz .LBB0_1711
	v_mbcnt_lo_u32_b32 v0, -1, 0
	v_mbcnt_hi_u32_b32 v200, -1, v0
	v_mov_b32_e32 v0, v200
	s_cmpk_gt_i32 s96, 0xaf
	s_cbranch_scc1 .LBB0_1711
	s_add_u32 s30, s88, 0x1c00000
	s_addc_u32 s31, s89, 0
	s_lshl_b32 s2, s95, 10
	v_lshl_add_u32 v1, v0, 4, s2
	v_ashrrev_i32_e32 v2, 31, v1
	v_lshrrev_b32_e32 v2, 22, v2
	v_add_u32_e32 v2, v1, v2
	v_ashrrev_i32_e32 v2, 10, v2
	v_mul_i32_i24_e32 v3, 0x400, v2
	v_sub_u32_e32 v1, v1, v3
	v_lshrrev_b32_e32 v3, 4, v1
	v_bitop3_b32 v1, v3, v1, 32 bitop3:0x6c
	v_ashrrev_i32_e32 v4, 31, v1
	s_add_i32 s33, s2, 0
	s_ashr_i32 s2, s96, 31
	v_lshrrev_b32_e32 v4, 26, v4
	s_lshr_b32 s2, s2, 30
	v_lshlrev_b32_e32 v3, 3, v2
	v_add_u32_e32 v4, v1, v4
	s_add_i32 s2, s96, s2
	v_and_b32_e32 v3, -16, v3
	v_ashrrev_i32_e32 v5, 6, v4
	s_ashr_i32 s16, s2, 2
	v_add_u32_e32 v3, v5, v3
	v_and_b32_e32 v5, 3, v5
	s_mov_b32 s3, 0x3fffe0
	s_and_b32 s2, s2, -4
	s_ashr_i32 s17, s16, 31
	s_lshr_b32 s4, s94, 8
	v_and_b32_e32 v4, 0xc0, v4
	v_and_or_b32 v5, v3, s3, v5
	s_sub_i32 s18, s96, s2
	s_lshl_b64 s[2:3], s[16:17], 18
	v_readlane_b32 s6, v254, 49
	v_sub_u32_e32 v1, v1, v4
	v_mov_b32_e32 v4, 1
	v_readlane_b32 s7, v254, 50
	s_add_u32 s22, s6, s2
	v_lshlrev_b32_e32 v2, 5, v2
	v_ashrrev_i16_sdwa v1, v4, sext(v1) dst_sel:DWORD dst_unused:UNUSED_PAD src0_sel:DWORD src1_sel:BYTE_0
	v_lshlrev_b32_e32 v4, 1, v3
	v_lshrrev_b32_e32 v6, 2, v3
	s_addc_u32 s23, s7, s3
	s_ashr_i32 s19, s18, 31
	v_and_b32_e32 v2, 32, v2
	v_bfe_i32 v1, v1, 0, 16
	v_and_b32_e32 v4, 24, v4
	v_and_b32_e32 v6, 4, v6
	s_lshl_b64 s[2:3], s[18:19], 18
	v_or3_b32 v4, v5, v6, v4
	v_add_lshl_u32 v1, v2, v1, 1
	s_add_u32 s20, s30, s2
	v_lshl_add_u32 v201, v4, 10, v1
	s_addc_u32 s21, s31, s3
	s_add_i32 s17, s33, 0x10000
	s_mov_b32 s2, m0
	s_mov_b32 m0, s17
	s_nop 0
	global_load_lds_dwordx4 v201, s[20:21]
	s_mov_b32 m0, s2
	s_add_u32 s2, s20, 0x10000
	s_addc_u32 s3, s21, 0
	s_add_i32 s19, s33, 0x12000
	s_mov_b32 s5, m0
	s_mov_b32 m0, s19
	s_nop 0
	global_load_lds_dwordx4 v201, s[2:3]
	s_mov_b32 m0, s5
	s_add_u32 s2, s20, 0x20000
	s_addc_u32 s3, s21, 0
	s_add_i32 s34, s33, 0x14000
	s_mov_b32 s5, m0
	s_mov_b32 m0, s34
	s_nop 0
	global_load_lds_dwordx4 v201, s[2:3]
	s_mov_b32 m0, s5
	s_add_u32 s2, s20, 0x30000
	s_addc_u32 s3, s21, 0
	s_add_i32 s35, s33, 0x16000
	s_mov_b32 s5, m0
	s_mov_b32 m0, s35
	s_nop 0
	global_load_lds_dwordx4 v201, s[2:3]
	s_mov_b32 m0, s5
	v_lshl_add_u32 v202, v3, 10, v1
	s_mov_b32 s2, m0
	s_mov_b32 m0, s33
	s_nop 0
	global_load_lds_dwordx4 v202, s[22:23]
	s_mov_b32 m0, s2
	s_add_u32 s2, s22, 0x10000
	s_addc_u32 s3, s23, 0
	s_add_i32 s36, s33, 0x2000
	s_mov_b32 s5, m0
	s_mov_b32 m0, s36
	s_nop 0
	global_load_lds_dwordx4 v202, s[2:3]
	s_mov_b32 m0, s5
	s_add_u32 s2, s22, 0x20000
	s_addc_u32 s3, s23, 0
	s_add_i32 s37, s33, 0x4000
	s_mov_b32 s5, m0
	s_mov_b32 m0, s37
	s_nop 0
	global_load_lds_dwordx4 v202, s[2:3]
	s_mov_b32 m0, s5
	s_add_u32 s6, s22, 0x30000
	s_addc_u32 s7, s23, 0
	s_add_i32 s38, s33, 0x6000
	s_mov_b32 s5, m0
	s_mov_b32 m0, s38
	s_nop 0
	global_load_lds_dwordx4 v202, s[6:7]
	s_mov_b32 m0, s5
	s_cmp_eq_u32 s4, 1
	s_cselect_b64 s[2:3], -1, 0
	s_cmp_lg_u32 s4, 1
	s_cbranch_scc1 .LBB0_1696
	s_barrier

.LBB0_1711:
	s_cmp_lt_u32 s96, 176
	s_cbranch_scc1 .Ltc_skip_10
	v_writelane_b32 v200, s0, 0
	s_nop 1
	v_writelane_b32 v200, s1, 1
	s_nop 1
	v_writelane_b32 v200, s2, 2
	s_nop 1
	v_writelane_b32 v200, s3, 3
	s_nop 1
	v_writelane_b32 v200, s4, 4
	s_nop 1
	v_writelane_b32 v200, s5, 5
	s_nop 1
	v_writelane_b32 v200, s6, 6
	s_nop 1
	v_writelane_b32 v200, s7, 7
	s_nop 1
	v_writelane_b32 v200, s10, 8
	s_nop 1
	v_writelane_b32 v200, s11, 9
	s_nop 1
	v_writelane_b32 v200, s12, 10
	s_nop 1
	v_writelane_b32 v200, s13, 11
	s_nop 1
	v_writelane_b32 v200, s14, 12
	s_nop 1
	v_writelane_b32 v200, s15, 13
	s_nop 1
	v_writelane_b32 v200, s16, 14
	s_nop 1
	v_writelane_b32 v200, s17, 15
	s_nop 1
	v_writelane_b32 v200, s18, 16
	s_nop 1
	v_writelane_b32 v200, s19, 17
	s_nop 1
	v_writelane_b32 v200, s20, 18
	s_nop 1
	v_writelane_b32 v200, s21, 19
	s_nop 1
	v_writelane_b32 v200, s22, 20
	s_nop 1
	v_writelane_b32 v200, s23, 21
	s_nop 1
	v_writelane_b32 v200, s24, 22
	s_nop 1
	v_writelane_b32 v200, s25, 23
	s_nop 1
	v_writelane_b32 v200, s36, 24
	s_nop 1
	v_writelane_b32 v200, s37, 25
	s_nop 1
	v_writelane_b32 v200, s38, 26
	s_nop 1
	v_writelane_b32 v200, s39, 27
	s_nop 1
	v_writelane_b32 v200, s40, 28
	s_nop 1
	v_writelane_b32 v200, s41, 29
	s_nop 1
	v_writelane_b32 v200, s42, 30
	s_nop 1
	v_writelane_b32 v200, s43, 31
	s_nop 1
	v_writelane_b32 v200, s44, 32
	s_nop 1
	v_writelane_b32 v200, s45, 33
	s_nop 1
	v_writelane_b32 v200, s46, 34
	s_nop 1
	v_writelane_b32 v200, s47, 35
	s_nop 1
	v_writelane_b32 v200, s48, 36
	s_nop 1
	v_writelane_b32 v200, s49, 37
	s_nop 1
	v_writelane_b32 v200, s50, 38
	s_nop 1
	v_writelane_b32 v200, s51, 39
	s_nop 1
	s_mov_b32 s99, 10
	s_mov_b32 s98, 6
	s_mov_b32 s101, 80
	s_add_i32 s100, s96, 3356
	s_branch .Ltc_s1_back

.LBB0_2020:
	s_cmp_lt_u32 s96, 144
	s_cbranch_scc1 .Ltc_skip_11
	v_writelane_b32 v200, s0, 0
	s_nop 1
	v_writelane_b32 v200, s1, 1
	s_nop 1
	v_writelane_b32 v200, s2, 2
	s_nop 1
	v_writelane_b32 v200, s3, 3
	s_nop 1
	v_writelane_b32 v200, s4, 4
	s_nop 1
	v_writelane_b32 v200, s5, 5
	s_nop 1
	v_writelane_b32 v200, s6, 6
	s_nop 1
	v_writelane_b32 v200, s7, 7
	s_nop 1
	v_writelane_b32 v200, s10, 8
	s_nop 1
	v_writelane_b32 v200, s11, 9
	s_nop 1
	v_writelane_b32 v200, s12, 10
	s_nop 1
	v_writelane_b32 v200, s13, 11
	s_nop 1
	v_writelane_b32 v200, s14, 12
	s_nop 1
	v_writelane_b32 v200, s15, 13
	s_nop 1
	v_writelane_b32 v200, s16, 14
	s_nop 1
	v_writelane_b32 v200, s17, 15
	s_nop 1
	v_writelane_b32 v200, s18, 16
	s_nop 1
	v_writelane_b32 v200, s19, 17
	s_nop 1
	v_writelane_b32 v200, s20, 18
	s_nop 1
	v_writelane_b32 v200, s21, 19
	s_nop 1
	v_writelane_b32 v200, s22, 20
	s_nop 1
	v_writelane_b32 v200, s23, 21
	s_nop 1
	v_writelane_b32 v200, s24, 22
	s_nop 1
	v_writelane_b32 v200, s25, 23
	s_nop 1
	v_writelane_b32 v200, s36, 24
	s_nop 1
	v_writelane_b32 v200, s37, 25
	s_nop 1
	v_writelane_b32 v200, s38, 26
	s_nop 1
	v_writelane_b32 v200, s39, 27
	s_nop 1
	v_writelane_b32 v200, s40, 28
	s_nop 1
	v_writelane_b32 v200, s41, 29
	s_nop 1
	v_writelane_b32 v200, s42, 30
	s_nop 1
	v_writelane_b32 v200, s43, 31
	s_nop 1
	v_writelane_b32 v200, s44, 32
	s_nop 1
	v_writelane_b32 v200, s45, 33
	s_nop 1
	v_writelane_b32 v200, s46, 34
	s_nop 1
	v_writelane_b32 v200, s47, 35
	s_nop 1
	v_writelane_b32 v200, s48, 36
	s_nop 1
	v_writelane_b32 v200, s49, 37
	s_nop 1
	v_writelane_b32 v200, s50, 38
	s_nop 1
	v_writelane_b32 v200, s51, 39
	s_nop 1
	s_mov_b32 s99, 11
	s_mov_b32 s98, 2
	s_mov_b32 s101, 112
	s_add_i32 s100, s96, 3868
	s_branch .Ltc_s2_back

.LBB0_2137:
	v_readlane_b32 s0, v254, 0
	v_readlane_b32 s1, v254, 1
	s_load_dwordx2 s[0:1], s[0:1], 0xd8
	s_waitcnt lgkmcnt(0)
	s_cmp_lt_i32 s0, 25
	s_cselect_b64 s[0:1], -1, 0
	s_and_b64 s[0:1], s[0:1], s[2:3]
	s_andn2_b64 vcc, exec, s[0:1]
	s_cbranch_vccnz .LBB0_2154
	v_mbcnt_lo_u32_b32 v0, -1, 0
	s_waitcnt vmcnt(3)
	v_mbcnt_hi_u32_b32 v128, -1, v0
	v_mov_b32_e32 v0, v128
	s_cmpk_gt_i32 s96, 0xc5
	s_cbranch_scc1 .LBB0_2154
	s_add_u32 s33, s88, 0x580000
	s_addc_u32 s34, s89, 0
	s_add_u32 s35, s88, 0x82300000
	s_addc_u32 s36, s89, 0
	s_lshl_b32 s3, s95, 10
	v_lshlrev_b32_e32 v1, 4, v0
	v_add_u32_e32 v2, s3, v1
	v_ashrrev_i32_e32 v3, 31, v2
	v_lshrrev_b32_e32 v3, 22, v3
	v_add_u32_e32 v3, v2, v3
	v_ashrrev_i32_e32 v3, 10, v3
	v_mul_i32_i24_e32 v4, 0x400, v3
	s_add_i32 s37, s3, 0
	s_mul_hi_i32 s3, s96, 0x2aaaaaab
	v_sub_u32_e32 v2, v2, v4
	s_lshr_b32 s4, s3, 31
	v_lshrrev_b32_e32 v4, 4, v2
	s_add_i32 s20, s3, s4
	v_bitop3_b32 v2, v4, v2, 32 bitop3:0x6c
	s_mul_i32 s3, s20, -6
	s_ashr_i32 s21, s20, 31
	s_lshr_b32 s2, s94, 8
	v_ashrrev_i32_e32 v5, 31, v2
	s_add_i32 s4, s3, s96
	s_lshl_b64 s[6:7], s[20:21], 18
	v_lshrrev_b32_e32 v5, 26, v5
	s_add_u32 s24, s35, s6
	v_add_u32_e32 v5, v2, v5
	s_addc_u32 s25, s36, s7
	s_ashr_i32 s5, s4, 31
	v_lshrrev_b32_e32 v6, 6, v5
	v_and_b32_e32 v5, 0xc0, v5
	s_lshl_b64 s[6:7], s[4:5], 18
	v_lshlrev_b32_e32 v4, 3, v3
	v_lshlrev_b32_e32 v3, 5, v3
	v_sub_u32_e32 v2, v2, v5
	v_mov_b32_e32 v5, 1
	s_add_u32 s22, s33, s6
	v_and_b32_e32 v4, 0x3ffff0, v4
	v_and_b32_e32 v3, 32, v3
	v_ashrrev_i16_sdwa v2, v5, sext(v2) dst_sel:DWORD dst_unused:UNUSED_PAD src0_sel:DWORD src1_sel:BYTE_0
	s_addc_u32 s23, s34, s7
	s_add_i32 s21, s37, 0x10000
	v_add_u32_sdwa v2, v3, sext(v2) dst_sel:DWORD dst_unused:UNUSED_PAD src0_sel:DWORD src1_sel:WORD_0
	v_add_lshl_u32 v3, v6, v4, 10
	s_add_u32 s6, s22, 0x10000
	v_lshl_add_u32 v129, v2, 1, v3
	s_mov_b32 s3, m0
	s_mov_b32 m0, s21
	s_nop 0
	global_load_lds_dwordx4 v129, s[22:23]
	s_mov_b32 m0, s3
	s_addc_u32 s7, s23, 0
	s_add_i32 s38, s37, 0x12000
	s_mov_b32 s3, m0
	s_mov_b32 m0, s38
	s_nop 0
	global_load_lds_dwordx4 v129, s[6:7]
	s_mov_b32 m0, s3
	s_add_u32 s6, s22, 0x20000
	s_addc_u32 s7, s23, 0
	s_add_i32 s39, s37, 0x14000
	s_mov_b32 s3, m0
	s_mov_b32 m0, s39
	s_nop 0
	global_load_lds_dwordx4 v129, s[6:7]
	s_mov_b32 m0, s3
	s_add_u32 s6, s22, 0x30000
	s_addc_u32 s7, s23, 0
	s_add_i32 s40, s37, 0x16000
	s_mov_b32 s3, m0
	s_mov_b32 m0, s40
	s_nop 0
	global_load_lds_dwordx4 v129, s[6:7]
	s_mov_b32 m0, s3
	s_add_u32 s6, s24, 0x10000
	s_mov_b32 s3, m0
	s_mov_b32 m0, s37
	s_nop 0
	global_load_lds_dwordx4 v129, s[24:25]
	s_mov_b32 m0, s3
	s_addc_u32 s7, s25, 0
	s_add_i32 s41, s37, 0x2000
	s_mov_b32 s3, m0
	s_mov_b32 m0, s41
	s_nop 0
	global_load_lds_dwordx4 v129, s[6:7]
	s_mov_b32 m0, s3
	s_add_u32 s6, s24, 0x20000
	s_addc_u32 s7, s25, 0
	s_add_i32 s42, s37, 0x4000
	s_mov_b32 s3, m0
	s_mov_b32 m0, s42
	s_nop 0
	global_load_lds_dwordx4 v129, s[6:7]
	s_mov_b32 m0, s3
	s_add_u32 s8, s24, 0x30000
	s_addc_u32 s9, s25, 0
	s_add_i32 s43, s37, 0x6000
	s_mov_b32 s3, m0
	s_mov_b32 m0, s43
	s_nop 0
	global_load_lds_dwordx4 v129, s[8:9]
	s_mov_b32 m0, s3
	s_cmp_eq_u32 s2, 1
	s_cselect_b64 s[6:7], -1, 0
	s_cmp_lg_u32 s2, 1
	s_cbranch_scc1 .LBB0_2141
	s_barrier

.LBB0_2154:
	s_cmp_lt_u32 s96, 198
	s_cbranch_scc1 .Ltc_skip_12
	v_writelane_b32 v200, s0, 0
	s_nop 1
	v_writelane_b32 v200, s1, 1
	s_nop 1
	v_writelane_b32 v200, s2, 2
	s_nop 1
	v_writelane_b32 v200, s3, 3
	s_nop 1
	v_writelane_b32 v200, s4, 4
	s_nop 1
	v_writelane_b32 v200, s5, 5
	s_nop 1
	v_writelane_b32 v200, s6, 6
	s_nop 1
	v_writelane_b32 v200, s7, 7
	s_nop 1
	v_writelane_b32 v200, s10, 8
	s_nop 1
	v_writelane_b32 v200, s11, 9
	s_nop 1
	v_writelane_b32 v200, s12, 10
	s_nop 1
	v_writelane_b32 v200, s13, 11
	s_nop 1
	v_writelane_b32 v200, s14, 12
	s_nop 1
	v_writelane_b32 v200, s15, 13
	s_nop 1
	v_writelane_b32 v200, s16, 14
	s_nop 1
	v_writelane_b32 v200, s17, 15
	s_nop 1
	v_writelane_b32 v200, s18, 16
	s_nop 1
	v_writelane_b32 v200, s19, 17
	s_nop 1
	v_writelane_b32 v200, s20, 18
	s_nop 1
	v_writelane_b32 v200, s21, 19
	s_nop 1
	v_writelane_b32 v200, s22, 20
	s_nop 1
	v_writelane_b32 v200, s23, 21
	s_nop 1
	v_writelane_b32 v200, s24, 22
	s_nop 1
	v_writelane_b32 v200, s25, 23
	s_nop 1
	v_writelane_b32 v200, s36, 24
	s_nop 1
	v_writelane_b32 v200, s37, 25
	s_nop 1
	v_writelane_b32 v200, s38, 26
	s_nop 1
	v_writelane_b32 v200, s39, 27
	s_nop 1
	v_writelane_b32 v200, s40, 28
	s_nop 1
	v_writelane_b32 v200, s41, 29
	s_nop 1
	v_writelane_b32 v200, s42, 30
	s_nop 1
	v_writelane_b32 v200, s43, 31
	s_nop 1
	v_writelane_b32 v200, s44, 32
	s_nop 1
	v_writelane_b32 v200, s45, 33
	s_nop 1
	v_writelane_b32 v200, s46, 34
	s_nop 1
	v_writelane_b32 v200, s47, 35
	s_nop 1
	v_writelane_b32 v200, s48, 36
	s_nop 1
	v_writelane_b32 v200, s49, 37
	s_nop 1
	v_writelane_b32 v200, s50, 38
	s_nop 1
	v_writelane_b32 v200, s51, 39
	s_nop 1
	s_mov_b32 s99, 12
	s_mov_b32 s98, 11
	s_mov_b32 s101, 58
	s_add_i32 s100, s96, 4038
	s_branch .Ltc_s2_back
